# E23: E19 + the same wave-group-0 exit-barrier deferral in the input-projection GEMM (flag-guarded, placed before each epilogue variant's parameter wait)
# speedup vs baseline: 1.0005x; 1.0005x over previous
.LBB0_156:
	s_lshl_b32 s44, s12, 6
	s_lshl_b32 s16, s12, 13
	s_mov_b64 s[12:13], 0x80
	s_and_b32 s5, s5, 3
	s_add_i32 m0, s40, 0x18000
	v_lshl_add_u64 v[8:9], v[8:9], 0, s[12:13]
	s_lshl_b32 s22, s5, 5
	s_lshl_b32 s17, s5, 12
	s_waitcnt vmcnt(2)
	s_barrier
	global_load_lds_dwordx4 v[8:9], off
	v_lshl_add_u64 v[6:7], v[6:7], 0, s[12:13]
	s_add_i32 m0, s40, 0x1a000
	s_add_i32 s45, s40, 0x8000
	s_add_i32 s46, s40, 0xa000
	global_load_lds_dwordx4 v[6:7], off
	v_lshl_add_u64 v[2:3], v[2:3], 0, s[12:13]
	s_mov_b32 m0, s45
	s_add_u32 s14, s6, 0x40080
	global_load_lds_dwordx4 v[2:3], off
	v_lshl_add_u64 v[2:3], v[4:5], 0, s[12:13]
	s_mov_b32 m0, s46
	s_addc_u32 s15, s7, 0
	global_load_lds_dwordx4 v[2:3], off
	s_add_i32 m0, s40, 0x1c000
	v_lshl_add_u64 v[2:3], s[14:15], 0, v[148:149]
	global_load_lds_dwordx4 v[2:3], off
	v_lshl_add_u64 v[2:3], s[14:15], 0, v[152:153]
	s_add_i32 m0, s40, 0x1e000
	v_bfe_u32 v0, v10, 4, 2
	global_load_lds_dwordx4 v[2:3], off
	v_and_b32_e32 v1, 15, v10
	v_lshlrev_b32_e32 v2, 4, v0
	v_lshlrev_b32_e32 v4, 2, v10
	v_or_b32_e32 v156, s44, v1
	v_lshl_or_b32 v3, v1, 6, v2
	v_and_b32_e32 v4, 32, v4
	s_cmpk_lt_u32 s4, 0x100
	v_lshl_or_b32 v158, v0, 3, s22
	v_readlane_b32 s20, v252, 2
	v_and_b32_e32 v0, 16, v2
	v_lshrrev_b32_e32 v2, 3, v10
	v_bitop3_b32 v5, v3, s16, v4 bitop3:0xde
	s_cselect_b64 s[14:15], -1, 0
	v_readlane_b32 s21, v252, 3
	s_add_u32 s16, s20, 0x36490a00
	v_and_b32_e32 v2, 4, v2
	v_ashrrev_i32_e32 v157, 31, v156
	v_bitop3_b32 v159, v3, s17, v4 bitop3:0xde
	s_addc_u32 s17, s21, 0
	v_lshlrev_b64 v[160:161], 13, v[156:157]
	v_or3_b32 v157, v0, v2, s22
	v_lshlrev_b32_e32 v0, 14, v11
	s_add_u32 s18, s20, 0x50490a00
	v_and_b32_e32 v0, 0xffff8000, v0
	s_addc_u32 s19, s21, 0
	v_lshl_add_u32 v0, v12, 11, v0
	v_and_b32_e32 v2, 1, v11
	s_add_u32 s47, s20, 0x3a490a00
	v_lshl_or_b32 v0, v2, 6, v0
	s_addc_u32 s48, s21, 0
	v_lshl_add_u32 v176, v13, 1, v0
	v_lshlrev_b32_e32 v0, 14, v14
	s_cmp_gt_u32 s5, 1
	v_readlane_b32 s4, v252, 6
	v_and_b32_e32 v0, 0xffff8000, v0
	s_waitcnt vmcnt(6)
	v_or_b32_e32 v162, 16, v156
	v_or_b32_e32 v166, 32, v156
	v_or_b32_e32 v170, 48, v156
	v_readlane_b32 s5, v252, 7
	v_lshl_add_u32 v0, v15, 11, v0
	v_and_b32_e32 v2, 1, v14
	v_ashrrev_i32_e32 v163, 31, v162
	v_ashrrev_i32_e32 v167, 31, v166
	v_ashrrev_i32_e32 v171, 31, v170
	s_cselect_b64 s[20:21], -1, 0
	v_lshlrev_b32_e32 v154, 2, v158
	s_ashr_i32 s49, s4, 31
	v_readlane_b32 s4, v252, 0
	v_lshl_or_b32 v0, v2, 6, v0
	s_add_i32 s51, 0, 0x10000
	s_add_i32 s52, 0, 0x14000
	v_lshlrev_b64 v[164:165], 13, v[162:163]
	v_lshlrev_b64 v[168:169], 13, v[166:167]
	v_lshlrev_b64 v[172:173], 13, v[170:171]
	v_lshl_add_u64 v[174:175], s[2:3], 0, v[154:155]
	s_ashr_i32 s50, s4, 31
	v_mov_b32_e32 v177, v155
	v_lshl_add_u32 v178, v16, 1, v0
	v_mov_b32_e32 v179, v155
	v_mov_b64_e32 v[180:181], 0xb80
	v_mov_b64_e32 v[182:183], 0xb7f
	v_add_u32_e32 v163, s51, v159
	v_add_u32_e32 v167, s52, v159
	v_add_u32_e32 v171, 0, v5
	s_mov_b32 s53, 0
	s_barrier
	v_readlane_b32 s5, v252, 1
	s_mov_b64 s[98:99], 0
	s_branch .LBB0_159
	s_nop 0
	s_nop 0
	s_nop 0
	s_nop 0
	s_nop 0
	s_nop 0
	s_nop 0
	s_nop 0
	s_nop 0
	s_nop 0
	s_nop 0
	s_nop 0
	s_nop 0
	s_nop 0
	s_nop 0

.Lkexit_162:
	s_and_b64 s[98:99], exec, s[14:15]
.LBB0_165:
	s_cmp_lg_u32 s8, 0
	s_cbranch_scc0 .LBB0_167
	s_cmp_eq_u32 s58, 21
	s_mov_b32 s0, 0x4e490a00
	s_cselect_b32 s0, s0, 0x4f490a00
	s_lshl_b32 s1, s57, 8
	v_or_b32_e32 v130, s1, v158
	v_lshl_add_u32 v184, s58, 8, v156
	v_ashrrev_i32_e32 v131, 31, v130
	v_ashrrev_i32_e32 v185, 31, v184
	v_lshl_add_u64 v[130:131], v[130:131], 2, s[16:17]
	v_lshl_add_u64 v[186:187], v[184:185], 2, s[2:3]
	global_load_dword v192, v[186:187], off
	global_load_dwordx4 v[142:145], v[130:131], off
	global_load_dwordx4 v[138:141], v[130:131], off offset:16
	global_load_dwordx4 v[134:137], v[130:131], off offset:512
	s_nop 0
	global_load_dwordx4 v[130:133], v[130:131], off offset:528
	s_nop 0
	global_load_dword v194, v[186:187], off offset:64
	v_add_u32_e32 v184, 0x80, v184
	v_ashrrev_i32_e32 v185, 31, v184
	v_lshl_add_u64 v[184:185], v[184:185], 2, s[2:3]
	global_load_dword v222, v[186:187], off offset:128
	global_load_dword v200, v[186:187], off offset:192
	global_load_dword v196, v[184:185], off
	global_load_dword v188, v[184:185], off offset:64
	s_nop 0
	global_load_dword v186, v[184:185], off offset:128
	s_nop 0
	global_load_dword v184, v[184:185], off offset:192
	v_readlane_b32 s6, v252, 2
	v_readlane_b32 s7, v252, 3
	s_add_u32 s6, s6, s0
	v_cvt_f32_i32_e32 v203, v127
	v_cvt_f32_i32_e32 v202, v126
	v_cvt_f32_i32_e32 v205, v123
	v_cvt_f32_i32_e32 v204, v122
	v_cvt_f32_i32_e32 v207, v129
	v_cvt_f32_i32_e32 v206, v128
	v_cvt_f32_i32_e32 v209, v125
	v_cvt_f32_i32_e32 v208, v124
	v_cvt_f32_i32_e32 v217, v117
	v_cvt_f32_i32_e32 v216, v116
	s_addc_u32 s7, s7, 0
	s_ashr_i32 s8, s57, 3
	v_cvt_f32_i32_e32 v211, v119
	v_cvt_f32_i32_e32 v210, v118
	v_cvt_f32_i32_e32 v213, v115
	v_cvt_f32_i32_e32 v212, v114
	v_cvt_f32_i32_e32 v215, v121
	v_cvt_f32_i32_e32 v214, v120
	s_and_b32 s1, s1, 0xf00
	s_and_b32 s0, s8, -2
	v_or_b32_e32 v0, s1, v157
	s_ashr_i32 s1, s0, 31
	v_lshl_add_u64 v[198:199], s[6:7], 0, v[160:161]
	s_lshl_b64 s[0:1], s[0:1], 20
	v_lshlrev_b32_e32 v154, 1, v0
	v_lshl_add_u64 v[224:225], v[198:199], 0, s[0:1]
	v_lshl_add_u64 v[224:225], v[224:225], 0, v[154:155]
	v_cvt_f32_i32_e32 v219, v111
	v_cvt_f32_i32_e32 v218, v110
	v_cvt_f32_i32_e32 v221, v107
	v_cvt_f32_i32_e32 v220, v106
	v_lshl_add_u64 v[190:191], s[6:7], 0, v[164:165]
	s_cmp_lg_u64 s[98:99], 0
	s_cbranch_scc0 .Lp1x0_a
	s_barrier
	s_mov_b64 s[98:99], 0
.Lp1x0_a:
	s_waitcnt vmcnt(0)
	v_pk_mul_f32 v[228:229], v[142:143], v[192:193] op_sel_hi:[1,0]
	v_pk_mul_f32 v[230:231], v[138:139], v[192:193] op_sel_hi:[1,0]
	v_pk_mul_f32 v[232:233], v[144:145], v[192:193] op_sel_hi:[1,0]
	v_pk_mul_f32 v[234:235], v[140:141], v[192:193] op_sel_hi:[1,0]
	v_pk_mul_f32 v[236:237], v[134:135], v[192:193] op_sel_hi:[1,0]
	v_pk_mul_f32 v[238:239], v[192:193], v[130:131] op_sel_hi:[0,1]
	v_pk_mul_f32 v[240:241], v[136:137], v[192:193] op_sel_hi:[1,0]
	v_pk_mul_f32 v[192:193], v[192:193], v[132:133] op_sel_hi:[0,1]
	v_pk_mul_f32 v[202:203], v[228:229], v[202:203]
	v_pk_mul_f32 v[204:205], v[230:231], v[204:205]
	v_pk_mul_f32 v[206:207], v[232:233], v[206:207]
	v_pk_mul_f32 v[208:209], v[234:235], v[208:209]
	v_pk_mul_f32 v[192:193], v[192:193], v[216:217]
	v_pk_mul_f32 v[210:211], v[236:237], v[210:211]
	v_pk_mul_f32 v[212:213], v[238:239], v[212:213]
	v_pk_mul_f32 v[214:215], v[240:241], v[214:215]
	v_cvt_pk_bf16_f32 v202, v202, v203
	v_cvt_pk_bf16_f32 v203, v206, v207
	v_cvt_pk_bf16_f32 v204, v204, v205
	v_cvt_pk_bf16_f32 v205, v208, v209
	v_cvt_pk_bf16_f32 v209, v192, v193
	v_cvt_f32_i32_e32 v193, v113
	v_cvt_f32_i32_e32 v192, v112
	v_cvt_pk_bf16_f32 v206, v210, v211
	v_cvt_pk_bf16_f32 v207, v214, v215
	v_cvt_pk_bf16_f32 v208, v212, v213
	global_store_dwordx2 v[224:225], v[202:203], off
	global_store_dwordx2 v[224:225], v[204:205], off offset:16
	global_store_dwordx2 v[224:225], v[206:207], off offset:256
	global_store_dwordx2 v[224:225], v[208:209], off offset:272
	v_cvt_f32_i32_e32 v203, v109
	v_cvt_f32_i32_e32 v202, v108
	v_pk_mul_f32 v[204:205], v[144:145], v[194:195] op_sel_hi:[1,0]
	v_pk_mul_f32 v[242:243], v[142:143], v[194:195] op_sel_hi:[1,0]
	v_pk_mul_f32 v[192:193], v[204:205], v[192:193]
	v_pk_mul_f32 v[204:205], v[140:141], v[194:195] op_sel_hi:[1,0]
	v_pk_mul_f32 v[244:245], v[138:139], v[194:195] op_sel_hi:[1,0]
	v_pk_mul_f32 v[202:203], v[204:205], v[202:203]
	v_pk_mul_f32 v[216:217], v[242:243], v[218:219]
	v_pk_mul_f32 v[218:219], v[244:245], v[220:221]
	v_cvt_pk_bf16_f32 v205, v192, v193
	v_cvt_pk_bf16_f32 v193, v202, v203
	v_lshl_add_u64 v[202:203], v[190:191], 0, s[0:1]
	v_cvt_pk_bf16_f32 v204, v216, v217
	v_cvt_pk_bf16_f32 v192, v218, v219
	v_lshl_add_u64 v[202:203], v[202:203], 0, v[154:155]
	global_store_dwordx2 v[202:203], v[204:205], off
	global_store_dwordx2 v[202:203], v[192:193], off offset:16
	v_cvt_f32_i32_e32 v193, v103
	v_cvt_f32_i32_e32 v192, v102
	v_cvt_f32_i32_e32 v205, v99
	v_cvt_f32_i32_e32 v204, v98
	v_pk_mul_f32 v[206:207], v[134:135], v[194:195] op_sel_hi:[1,0]
	v_cvt_f32_i32_e32 v209, v101
	v_pk_mul_f32 v[192:193], v[206:207], v[192:193]
	v_pk_mul_f32 v[206:207], v[130:131], v[194:195] op_sel_hi:[1,0]
	v_cvt_f32_i32_e32 v208, v100
	v_pk_mul_f32 v[204:205], v[206:207], v[204:205]
	v_cvt_f32_i32_e32 v207, v105
	v_cvt_f32_i32_e32 v206, v104
	v_pk_mul_f32 v[210:211], v[136:137], v[194:195] op_sel_hi:[1,0]
	v_pk_mul_f32 v[194:195], v[132:133], v[194:195] op_sel_hi:[1,0]
	v_cvt_pk_bf16_f32 v192, v192, v193
	v_pk_mul_f32 v[206:207], v[210:211], v[206:207]
	v_pk_mul_f32 v[194:195], v[194:195], v[208:209]
	v_cvt_pk_bf16_f32 v193, v206, v207
	v_cvt_pk_bf16_f32 v204, v204, v205
	v_cvt_pk_bf16_f32 v205, v194, v195
	v_cvt_f32_i32_e32 v195, v95
	v_cvt_f32_i32_e32 v194, v94
	global_store_dwordx2 v[202:203], v[192:193], off offset:256
	global_store_dwordx2 v[202:203], v[204:205], off offset:272
	v_cvt_f32_i32_e32 v203, v91
	v_cvt_f32_i32_e32 v202, v90
	v_pk_mul_f32 v[204:205], v[142:143], v[222:223] op_sel_hi:[1,0]
	v_cvt_f32_i32_e32 v207, v93
	v_pk_mul_f32 v[194:195], v[204:205], v[194:195]
	v_pk_mul_f32 v[204:205], v[138:139], v[222:223] op_sel_hi:[1,0]
	v_cvt_f32_i32_e32 v206, v92
	v_pk_mul_f32 v[202:203], v[204:205], v[202:203]
	v_cvt_f32_i32_e32 v205, v97
	v_cvt_f32_i32_e32 v204, v96
	v_pk_mul_f32 v[208:209], v[144:145], v[222:223] op_sel_hi:[1,0]
	v_lshl_add_u64 v[192:193], s[6:7], 0, v[168:169]
	v_cvt_pk_bf16_f32 v194, v194, v195
	v_pk_mul_f32 v[204:205], v[208:209], v[204:205]
	v_pk_mul_f32 v[208:209], v[140:141], v[222:223] op_sel_hi:[1,0]
	v_cvt_pk_bf16_f32 v195, v204, v205
	v_lshl_add_u64 v[204:205], v[192:193], 0, s[0:1]
	v_pk_mul_f32 v[206:207], v[208:209], v[206:207]
	v_lshl_add_u64 v[204:205], v[204:205], 0, v[154:155]
	v_cvt_pk_bf16_f32 v202, v202, v203
	v_cvt_pk_bf16_f32 v203, v206, v207
	global_store_dwordx2 v[204:205], v[194:195], off
	global_store_dwordx2 v[204:205], v[202:203], off offset:16
	v_cvt_f32_i32_e32 v195, v87
	v_cvt_f32_i32_e32 v194, v86
	v_cvt_f32_i32_e32 v203, v83
	v_cvt_f32_i32_e32 v202, v82
	v_pk_mul_f32 v[206:207], v[134:135], v[222:223] op_sel_hi:[1,0]
	v_cvt_f32_i32_e32 v209, v85
	v_pk_mul_f32 v[194:195], v[206:207], v[194:195]
	v_pk_mul_f32 v[206:207], v[130:131], v[222:223] op_sel_hi:[1,0]
	v_cvt_f32_i32_e32 v208, v84
	v_pk_mul_f32 v[202:203], v[206:207], v[202:203]
	v_cvt_f32_i32_e32 v207, v89
	v_cvt_f32_i32_e32 v206, v88
	v_pk_mul_f32 v[210:211], v[136:137], v[222:223] op_sel_hi:[1,0]
	v_cvt_pk_bf16_f32 v194, v194, v195
	v_cvt_pk_bf16_f32 v202, v202, v203
	v_pk_mul_f32 v[206:207], v[210:211], v[206:207]
	v_pk_mul_f32 v[210:211], v[132:133], v[222:223] op_sel_hi:[1,0]
	v_cvt_pk_bf16_f32 v195, v206, v207
	v_pk_mul_f32 v[208:209], v[210:211], v[208:209]
	v_pk_mul_f32 v[206:207], v[142:143], v[200:201] op_sel_hi:[1,0]
	v_cvt_pk_bf16_f32 v203, v208, v209
	global_store_dwordx2 v[204:205], v[194:195], off offset:256
	global_store_dwordx2 v[204:205], v[202:203], off offset:272
	v_cvt_f32_i32_e32 v203, v79
	v_cvt_f32_i32_e32 v202, v78
	v_cvt_f32_i32_e32 v205, v75
	v_cvt_f32_i32_e32 v204, v74
	v_cvt_f32_i32_e32 v209, v77
	v_pk_mul_f32 v[202:203], v[206:207], v[202:203]
	v_pk_mul_f32 v[206:207], v[138:139], v[200:201] op_sel_hi:[1,0]
	v_cvt_f32_i32_e32 v208, v76
	v_pk_mul_f32 v[204:205], v[206:207], v[204:205]
	v_cvt_f32_i32_e32 v207, v81
	v_cvt_f32_i32_e32 v206, v80
	v_pk_mul_f32 v[210:211], v[144:145], v[200:201] op_sel_hi:[1,0]
	v_lshl_add_u64 v[194:195], s[6:7], 0, v[172:173]
	v_cvt_pk_bf16_f32 v202, v202, v203
	v_pk_mul_f32 v[206:207], v[210:211], v[206:207]
	v_pk_mul_f32 v[210:211], v[140:141], v[200:201] op_sel_hi:[1,0]
	v_cvt_pk_bf16_f32 v203, v206, v207
	v_lshl_add_u64 v[206:207], v[194:195], 0, s[0:1]
	v_pk_mul_f32 v[208:209], v[210:211], v[208:209]
	v_lshl_add_u64 v[206:207], v[206:207], 0, v[154:155]
	v_cvt_pk_bf16_f32 v204, v204, v205
	v_cvt_pk_bf16_f32 v205, v208, v209
	global_store_dwordx2 v[206:207], v[202:203], off
	global_store_dwordx2 v[206:207], v[204:205], off offset:16
	v_cvt_f32_i32_e32 v203, v71
	v_cvt_f32_i32_e32 v202, v70
	v_cvt_f32_i32_e32 v205, v67
	v_cvt_f32_i32_e32 v204, v66
	v_pk_mul_f32 v[208:209], v[134:135], v[200:201] op_sel_hi:[1,0]
	v_cvt_f32_i32_e32 v211, v69
	v_pk_mul_f32 v[202:203], v[208:209], v[202:203]
	v_pk_mul_f32 v[208:209], v[130:131], v[200:201] op_sel_hi:[1,0]
	v_cvt_f32_i32_e32 v210, v68
	v_pk_mul_f32 v[204:205], v[208:209], v[204:205]
	v_cvt_f32_i32_e32 v209, v73
	v_cvt_f32_i32_e32 v208, v72
	v_pk_mul_f32 v[212:213], v[136:137], v[200:201] op_sel_hi:[1,0]
	v_pk_mul_f32 v[200:201], v[132:133], v[200:201] op_sel_hi:[1,0]
	v_cvt_pk_bf16_f32 v202, v202, v203
	v_pk_mul_f32 v[208:209], v[212:213], v[208:209]
	v_pk_mul_f32 v[200:201], v[200:201], v[210:211]
	v_cvt_pk_bf16_f32 v203, v208, v209
	v_cvt_pk_bf16_f32 v204, v204, v205
	v_cvt_pk_bf16_f32 v205, v200, v201
	v_cvt_f32_i32_e32 v201, v63
	v_cvt_f32_i32_e32 v200, v62
	global_store_dwordx2 v[206:207], v[202:203], off offset:256
	global_store_dwordx2 v[206:207], v[204:205], off offset:272
	v_cvt_f32_i32_e32 v203, v59
	v_cvt_f32_i32_e32 v202, v58
	v_pk_mul_f32 v[204:205], v[142:143], v[196:197] op_sel_hi:[1,0]
	v_cvt_f32_i32_e32 v207, v61
	v_pk_mul_f32 v[200:201], v[204:205], v[200:201]
	v_pk_mul_f32 v[204:205], v[138:139], v[196:197] op_sel_hi:[1,0]
	v_cvt_f32_i32_e32 v206, v60
	v_pk_mul_f32 v[202:203], v[204:205], v[202:203]
	v_cvt_f32_i32_e32 v205, v65
	v_cvt_f32_i32_e32 v204, v64
	s_or_b32 s0, s8, 1
	s_ashr_i32 s1, s0, 31
	v_pk_mul_f32 v[208:209], v[144:145], v[196:197] op_sel_hi:[1,0]
	s_lshl_b64 s[0:1], s[0:1], 20
	v_pk_mul_f32 v[204:205], v[208:209], v[204:205]
	v_pk_mul_f32 v[208:209], v[140:141], v[196:197] op_sel_hi:[1,0]
	v_lshl_add_u64 v[198:199], v[198:199], 0, s[0:1]
	v_pk_mul_f32 v[206:207], v[208:209], v[206:207]
	v_cvt_pk_bf16_f32 v200, v200, v201
	v_cvt_pk_bf16_f32 v201, v204, v205
	v_lshl_add_u64 v[198:199], v[198:199], 0, v[154:155]
	v_cvt_pk_bf16_f32 v202, v202, v203
	v_cvt_pk_bf16_f32 v203, v206, v207
	global_store_dwordx2 v[198:199], v[200:201], off
	global_store_dwordx2 v[198:199], v[202:203], off offset:16
	v_cvt_f32_i32_e32 v201, v55
	v_cvt_f32_i32_e32 v200, v54
	v_cvt_f32_i32_e32 v203, v51
	v_cvt_f32_i32_e32 v202, v50
	v_pk_mul_f32 v[204:205], v[134:135], v[196:197] op_sel_hi:[1,0]
	v_cvt_f32_i32_e32 v207, v53
	v_pk_mul_f32 v[200:201], v[204:205], v[200:201]
	v_pk_mul_f32 v[204:205], v[130:131], v[196:197] op_sel_hi:[1,0]
	v_cvt_f32_i32_e32 v206, v52
	v_pk_mul_f32 v[202:203], v[204:205], v[202:203]
	v_cvt_f32_i32_e32 v205, v57
	v_cvt_f32_i32_e32 v204, v56
	v_pk_mul_f32 v[208:209], v[136:137], v[196:197] op_sel_hi:[1,0]
	v_pk_mul_f32 v[196:197], v[132:133], v[196:197] op_sel_hi:[1,0]
	v_cvt_pk_bf16_f32 v200, v200, v201
	v_pk_mul_f32 v[204:205], v[208:209], v[204:205]
	v_pk_mul_f32 v[196:197], v[196:197], v[206:207]
	v_cvt_pk_bf16_f32 v201, v204, v205
	v_cvt_pk_bf16_f32 v202, v202, v203
	v_cvt_pk_bf16_f32 v203, v196, v197
	v_cvt_f32_i32_e32 v197, v47
	v_cvt_f32_i32_e32 v196, v46
	global_store_dwordx2 v[198:199], v[200:201], off offset:256
	global_store_dwordx2 v[198:199], v[202:203], off offset:272
	v_cvt_f32_i32_e32 v199, v43
	v_cvt_f32_i32_e32 v198, v42
	v_pk_mul_f32 v[200:201], v[142:143], v[188:189] op_sel_hi:[1,0]
	v_cvt_f32_i32_e32 v203, v45
	v_pk_mul_f32 v[196:197], v[200:201], v[196:197]
	v_pk_mul_f32 v[200:201], v[138:139], v[188:189] op_sel_hi:[1,0]
	v_cvt_f32_i32_e32 v202, v44
	v_pk_mul_f32 v[198:199], v[200:201], v[198:199]
	v_cvt_f32_i32_e32 v201, v49
	v_cvt_f32_i32_e32 v200, v48
	v_pk_mul_f32 v[204:205], v[144:145], v[188:189] op_sel_hi:[1,0]
	v_lshl_add_u64 v[190:191], v[190:191], 0, s[0:1]
	v_cvt_pk_bf16_f32 v196, v196, v197
	v_pk_mul_f32 v[200:201], v[204:205], v[200:201]
	v_pk_mul_f32 v[204:205], v[140:141], v[188:189] op_sel_hi:[1,0]
	v_cvt_pk_bf16_f32 v197, v200, v201
	v_pk_mul_f32 v[202:203], v[204:205], v[202:203]
	v_lshl_add_u64 v[190:191], v[190:191], 0, v[154:155]
	v_cvt_pk_bf16_f32 v198, v198, v199
	v_cvt_pk_bf16_f32 v199, v202, v203
	global_store_dwordx2 v[190:191], v[196:197], off
	global_store_dwordx2 v[190:191], v[198:199], off offset:16
	v_cvt_f32_i32_e32 v197, v39
	v_cvt_f32_i32_e32 v196, v38
	v_cvt_f32_i32_e32 v199, v35
	v_cvt_f32_i32_e32 v198, v34
	v_pk_mul_f32 v[200:201], v[134:135], v[188:189] op_sel_hi:[1,0]
	v_cvt_f32_i32_e32 v203, v37
	v_pk_mul_f32 v[196:197], v[200:201], v[196:197]
	v_pk_mul_f32 v[200:201], v[130:131], v[188:189] op_sel_hi:[1,0]
	v_cvt_f32_i32_e32 v202, v36
	v_pk_mul_f32 v[198:199], v[200:201], v[198:199]
	v_cvt_f32_i32_e32 v201, v41
	v_cvt_f32_i32_e32 v200, v40
	v_pk_mul_f32 v[204:205], v[136:137], v[188:189] op_sel_hi:[1,0]
	v_pk_mul_f32 v[188:189], v[132:133], v[188:189] op_sel_hi:[1,0]
	v_cvt_pk_bf16_f32 v196, v196, v197
	v_pk_mul_f32 v[200:201], v[204:205], v[200:201]
	v_pk_mul_f32 v[188:189], v[188:189], v[202:203]
	v_cvt_pk_bf16_f32 v197, v200, v201
	v_cvt_pk_bf16_f32 v198, v198, v199
	v_cvt_pk_bf16_f32 v199, v188, v189
	v_cvt_f32_i32_e32 v189, v31
	v_cvt_f32_i32_e32 v188, v30
	global_store_dwordx2 v[190:191], v[196:197], off offset:256
	global_store_dwordx2 v[190:191], v[198:199], off offset:272
	v_cvt_f32_i32_e32 v191, v27
	v_cvt_f32_i32_e32 v190, v26
	v_pk_mul_f32 v[196:197], v[142:143], v[186:187] op_sel_hi:[1,0]
	v_cvt_f32_i32_e32 v199, v29
	v_pk_mul_f32 v[188:189], v[196:197], v[188:189]
	v_pk_mul_f32 v[196:197], v[138:139], v[186:187] op_sel_hi:[1,0]
	v_cvt_f32_i32_e32 v198, v28
	v_pk_mul_f32 v[190:191], v[196:197], v[190:191]
	v_cvt_f32_i32_e32 v197, v33
	v_cvt_f32_i32_e32 v196, v32
	v_pk_mul_f32 v[200:201], v[144:145], v[186:187] op_sel_hi:[1,0]
	v_lshl_add_u64 v[192:193], v[192:193], 0, s[0:1]
	v_cvt_pk_bf16_f32 v188, v188, v189
	v_pk_mul_f32 v[196:197], v[200:201], v[196:197]
	v_pk_mul_f32 v[200:201], v[140:141], v[186:187] op_sel_hi:[1,0]
	v_cvt_pk_bf16_f32 v189, v196, v197
	v_pk_mul_f32 v[198:199], v[200:201], v[198:199]
	v_lshl_add_u64 v[192:193], v[192:193], 0, v[154:155]
	v_cvt_pk_bf16_f32 v190, v190, v191
	v_cvt_pk_bf16_f32 v191, v198, v199
	global_store_dwordx2 v[192:193], v[188:189], off
	global_store_dwordx2 v[192:193], v[190:191], off offset:16
	v_cvt_f32_i32_e32 v189, v23
	v_cvt_f32_i32_e32 v188, v22
	v_cvt_f32_i32_e32 v191, v19
	v_cvt_f32_i32_e32 v190, v18
	v_pk_mul_f32 v[196:197], v[134:135], v[186:187] op_sel_hi:[1,0]
	v_cvt_f32_i32_e32 v199, v21
	v_pk_mul_f32 v[188:189], v[196:197], v[188:189]
	v_pk_mul_f32 v[196:197], v[130:131], v[186:187] op_sel_hi:[1,0]
	v_cvt_f32_i32_e32 v198, v20
	v_pk_mul_f32 v[190:191], v[196:197], v[190:191]
	v_cvt_f32_i32_e32 v197, v25
	v_cvt_f32_i32_e32 v196, v24
	v_pk_mul_f32 v[200:201], v[136:137], v[186:187] op_sel_hi:[1,0]
	v_pk_mul_f32 v[186:187], v[132:133], v[186:187] op_sel_hi:[1,0]
	v_cvt_pk_bf16_f32 v188, v188, v189
	v_pk_mul_f32 v[196:197], v[200:201], v[196:197]
	v_pk_mul_f32 v[186:187], v[186:187], v[198:199]
	v_cvt_pk_bf16_f32 v189, v196, v197
	v_cvt_pk_bf16_f32 v190, v190, v191
	v_cvt_pk_bf16_f32 v191, v186, v187
	global_store_dwordx2 v[192:193], v[188:189], off offset:256
	global_store_dwordx2 v[192:193], v[190:191], off offset:272
	v_cvt_f32_i32_e32 v189, v11
	v_cvt_f32_i32_e32 v188, v10
	v_cvt_f32_i32_e32 v187, v15
	v_cvt_f32_i32_e32 v186, v14
	v_pk_mul_f32 v[138:139], v[138:139], v[184:185] op_sel_hi:[1,0]
	v_pk_mul_f32 v[142:143], v[142:143], v[184:185] op_sel_hi:[1,0]
	v_pk_mul_f32 v[138:139], v[138:139], v[188:189]
	v_cvt_f32_i32_e32 v189, v13
	v_cvt_f32_i32_e32 v188, v12
	v_pk_mul_f32 v[142:143], v[142:143], v[186:187]
	v_cvt_f32_i32_e32 v187, v17
	v_cvt_f32_i32_e32 v186, v16
	v_pk_mul_f32 v[140:141], v[140:141], v[184:185] op_sel_hi:[1,0]
	v_pk_mul_f32 v[144:145], v[144:145], v[184:185] op_sel_hi:[1,0]
	v_pk_mul_f32 v[140:141], v[140:141], v[188:189]
	v_pk_mul_f32 v[144:145], v[144:145], v[186:187]
	v_cvt_pk_bf16_f32 v138, v138, v139
	v_cvt_pk_bf16_f32 v139, v140, v141
	v_lshl_add_u64 v[140:141], v[194:195], 0, s[0:1]
	v_cvt_pk_bf16_f32 v142, v142, v143
	v_cvt_pk_bf16_f32 v143, v144, v145
	v_lshl_add_u64 v[140:141], v[140:141], 0, v[154:155]
	global_store_dwordx2 v[140:141], v[142:143], off
	global_store_dwordx2 v[140:141], v[138:139], off offset:16
	v_cvt_f32_i32_e32 v139, v7
	v_cvt_f32_i32_e32 v138, v6
	v_cvt_f32_i32_e32 v143, v3
	v_cvt_f32_i32_e32 v142, v2
	v_pk_mul_f32 v[134:135], v[134:135], v[184:185] op_sel_hi:[1,0]
	v_pk_mul_f32 v[130:131], v[130:131], v[184:185] op_sel_hi:[1,0]
	v_pk_mul_f32 v[134:135], v[134:135], v[138:139]
	v_cvt_f32_i32_e32 v139, v9
	v_cvt_f32_i32_e32 v138, v8
	v_pk_mul_f32 v[130:131], v[130:131], v[142:143]
	v_cvt_f32_i32_e32 v143, v5
	v_cvt_f32_i32_e32 v142, v4
	v_pk_mul_f32 v[136:137], v[136:137], v[184:185] op_sel_hi:[1,0]
	v_pk_mul_f32 v[132:133], v[132:133], v[184:185] op_sel_hi:[1,0]
	v_pk_mul_f32 v[136:137], v[136:137], v[138:139]
	v_pk_mul_f32 v[132:133], v[132:133], v[142:143]
	v_cvt_pk_bf16_f32 v134, v134, v135
	v_cvt_pk_bf16_f32 v135, v136, v137
	v_cvt_pk_bf16_f32 v130, v130, v131
	v_cvt_pk_bf16_f32 v131, v132, v133
	global_store_dwordx2 v[140:141], v[134:135], off offset:256
	global_store_dwordx2 v[140:141], v[130:131], off offset:272
	s_cbranch_execz .LBB0_168
	s_branch .LBB0_243
	s_nop 0
	s_nop 0
	s_nop 0
	s_nop 0
	s_nop 0
	s_nop 0
	s_nop 0
	s_nop 0
	s_nop 0
	s_nop 0
	s_nop 0
	s_nop 0
	s_nop 0
	s_nop 0

.LBB0_199:
	v_cvt_f32_i32_e32 v127, v127
	v_cvt_f32_i32_e32 v126, v126
	v_cvt_f32_i32_e32 v129, v129
	v_cvt_f32_i32_e32 v128, v128
	v_cvt_f32_i32_e32 v123, v123
	v_cvt_f32_i32_e32 v122, v122
	s_cmp_lg_u64 s[98:99], 0
	s_cbranch_scc0 .Lp1x0_b
	s_barrier
	s_mov_b64 s[98:99], 0
.Lp1x0_b:
	s_waitcnt vmcnt(0)
	v_pk_mul_f32 v[204:205], v[142:143], v[200:201] op_sel_hi:[1,0]
	v_cvt_f32_i32_e32 v125, v125
	v_cvt_f32_i32_e32 v124, v124
	v_pk_mul_f32 v[126:127], v[204:205], v[126:127]
	v_pk_mul_f32 v[204:205], v[144:145], v[200:201] op_sel_hi:[1,0]
	v_lshlrev_b32_e32 v154, 1, v158
	v_pk_mul_f32 v[128:129], v[204:205], v[128:129]
	v_pk_mul_f32 v[204:205], v[138:139], v[200:201] op_sel_hi:[1,0]
	s_xor_b64 s[6:7], s[6:7], -1
	v_pk_mul_f32 v[204:205], v[204:205], v[122:123]
	v_pk_mul_f32 v[122:123], v[140:141], v[200:201] op_sel_hi:[1,0]
	v_lshl_add_u64 v[188:189], s[0:1], 0, v[154:155]
	v_pk_mul_f32 v[206:207], v[122:123], v[124:125]
	v_cndmask_b32_e64 v0, 0, 1, s[6:7]
	v_lshl_add_u64 v[202:203], v[202:203], 1, v[188:189]
	v_cvt_pk_bf16_f32 v122, v126, v127
	v_cvt_pk_bf16_f32 v123, v128, v129
	v_cvt_pk_bf16_f32 v124, v204, v205
	v_cvt_pk_bf16_f32 v125, v206, v207
	v_cmp_ne_u32_e64 s[0:1], 1, v0
	s_andn2_b64 vcc, exec, s[6:7]
	global_store_dwordx4 v[202:203], v[122:125], off
	s_cbranch_vccnz .LBB0_201
	v_cvt_f32_i32_e32 v119, v119
	v_cvt_f32_i32_e32 v118, v118
	v_cvt_f32_i32_e32 v121, v121
	v_cvt_f32_i32_e32 v120, v120
	v_mov_b32_e32 v201, v200
	v_cvt_f32_i32_e32 v115, v115
	v_cvt_f32_i32_e32 v114, v114
	v_pk_mul_f32 v[122:123], v[134:135], v[200:201]
	v_cvt_f32_i32_e32 v117, v117
	v_cvt_f32_i32_e32 v116, v116
	v_pk_mul_f32 v[118:119], v[122:123], v[118:119]
	v_pk_mul_f32 v[122:123], v[136:137], v[200:201]
	s_nop 0
	v_pk_mul_f32 v[120:121], v[122:123], v[120:121]
	v_pk_mul_f32 v[122:123], v[130:131], v[200:201]
	s_nop 0
	v_pk_mul_f32 v[122:123], v[122:123], v[114:115]
	v_pk_mul_f32 v[114:115], v[132:133], v[200:201]
	s_nop 0
	v_pk_mul_f32 v[124:125], v[114:115], v[116:117]
	v_cvt_pk_bf16_f32 v114, v118, v119
	v_cvt_pk_bf16_f32 v115, v120, v121
	v_cvt_pk_bf16_f32 v116, v122, v123
	v_cvt_pk_bf16_f32 v117, v124, v125
	v_lshl_add_u64 v[118:119], s[26:27], 1, v[202:203]
	global_store_dwordx4 v[118:119], v[114:117], off

.LBB0_243:
	s_cmp_lg_u64 s[98:99], 0
	s_cbranch_scc0 .Lp1x0_c
	s_barrier
	s_mov_b64 s[98:99], 0

.LBB0_248:
	v_readlane_b32 s0, v252, 6
	s_abs_i32 s0, s0
	v_readlane_b32 s1, v252, 7
	v_cvt_f32_u32_e32 v0, s0
	s_sub_i32 s1, 0, s0
	s_waitcnt vmcnt(0)
	v_mov_b32_e32 v39, v226
	v_rcp_iflag_f32_e32 v0, v0
	v_readfirstlane_b32 s3, v39
	v_and_b32_e32 v26, 63, v39
	v_mul_f32_e32 v0, 0x4f7ffffe, v0
	v_cvt_u32_f32_e32 v0, v0
	s_nop 0
	v_readfirstlane_b32 s2, v0
	s_mul_i32 s1, s1, s2
	s_mul_hi_u32 s1, s2, s1
	s_add_i32 s2, s2, s1
	s_mul_hi_u32 s1, s2, 0xb80
	s_mul_i32 s1, s1, s0
	s_sub_i32 s1, 0xb80, s1
	s_sub_i32 s2, s1, s0
	s_cmp_ge_u32 s1, s0
	s_cselect_b32 s1, s2, s1
	s_sub_i32 s2, s1, s0
	s_cmp_ge_u32 s1, s0
	s_cselect_b32 s2, s2, s1
	s_ashr_i32 s12, s3, 6
	s_cmp_lg_u32 s2, 0
	s_cbranch_scc0 .LBB0_276
	v_readlane_b32 s0, v252, 0
	s_cmp_lt_i32 s0, s2
	v_readlane_b32 s1, v252, 1
	s_cbranch_scc1 .LBB0_275
	v_readlane_b32 s0, v252, 0
	s_sub_i32 s0, s0, s2
	s_lshl_b32 s0, s0, 3
	s_add_i32 s13, s12, s0
	s_cmpk_gt_i32 s13, 0xabf
	v_readlane_b32 s1, v252, 1
	s_cbranch_scc1 .LBB0_275
	v_readlane_b32 s0, v252, 6
	s_sub_i32 s8, s0, s2
	s_lshl_b32 s14, s8, 3
	v_readlane_b32 s6, v252, 2
	v_readlane_b32 s1, v252, 7
	s_mov_b32 s18, s0
	v_readlane_b32 s7, v252, 3
	s_add_u32 s0, s6, 0x1a90a00
	v_lshlrev_b32_e32 v0, 3, v26
	s_addc_u32 s1, s7, 0
	s_lshl_b32 s4, s12, 14
	v_lshrrev_b32_e32 v43, 3, v26
	v_and_b32_e32 v34, 56, v0
	s_add_i32 s4, s4, 0
	v_and_b32_e32 v30, 31, v39
	v_mul_u32_u24_e32 v0, 0x84, v34
	v_mov_b32_e32 v37, 0
	v_lshlrev_b32_e32 v1, 2, v43
	v_lshlrev_b32_e32 v36, 2, v26
	v_lshl_add_u32 v32, v30, 2, s4
	v_add3_u32 v45, s4, v0, v1
	v_lshl_add_u64 v[2:3], s[6:7], 0, v[36:37]
	s_mov_b64 s[4:5], 0x22490a00
	v_lshl_add_u64 v[40:41], v[2:3], 0, s[4:5]
	s_add_u32 s4, s6, 0x6ca90a00
	s_addc_u32 s5, s7, 0
	s_add_u32 s6, s6, 0x6cab0a00
	v_readlane_b32 s10, v252, 0
	s_addc_u32 s7, s7, 0
	s_lshl_b32 s9, s10, 13
	s_lshl_b32 s10, s12, 10
	s_add_i32 s9, s9, s10
	v_and_b32_e32 v0, 32, v39
	v_or3_b32 v0, s9, v0, v30
	s_lshl_b32 s10, s2, 13
	v_lshrrev_b32_e32 v28, 5, v26
	v_lshlrev_b32_e32 v38, 11, v30
	v_subrev_u32_e32 v0, s10, v0
	v_add_u32_e32 v61, 0xffd60000, v0
	v_or_b32_e32 v0, v28, v38
	v_and_b32_e32 v2, 32, v26
	s_lshl_b32 s16, s8, 13
	v_or_b32_e32 v42, 4, v38
	v_or_b32_e32 v44, 8, v38
	v_or_b32_e32 v46, 12, v38
	v_lshl_add_u32 v0, s13, 5, v0
	s_lshl_b32 s8, s18, 8
	s_lshl_b32 s2, s2, 8
	v_or3_b32 v2, s9, v2, v30
	s_mov_b32 s3, 0
	s_movk_i32 s15, 0x84
	v_or_b32_e32 v47, 8, v43
	v_or_b32_e32 v58, 16, v43
	v_or_b32_e32 v59, 24, v43
	v_or_b32_e32 v60, 0xfffeb000, v28
	v_mov_b32_e32 v1, v28
	v_mov_b32_e32 v27, v30
	v_mov_b32_e32 v29, v38
	v_mov_b32_e32 v31, v42
	v_mov_b32_e32 v33, v44
	v_mov_b32_e32 v35, v46
	v_add_u32_e32 v62, 0xfffeb004, v0
	s_sub_i32 s17, s8, s2
	v_subrev_u32_e32 v63, s10, v2
	v_add_u32_e32 v48, 0xfffeb002, v0
	v_add_u32_e32 v50, 0xfffeb000, v0
	s_mov_b32 s18, 0x2290a00
	v_lshlrev_b32_e32 v52, 2, v26
	s_movk_i32 s19, 0x1000
	s_movk_i32 s20, 0x2000
	s_movk_i32 s21, 0x3000
	s_movk_i32 s22, 0x4000
	s_movk_i32 s23, 0x5000
	s_movk_i32 s24, 0x6000
	s_movk_i32 s25, 0x7000
	s_mov_b32 s26, 0x7ffffc40
	s_mov_b32 s27, 0x6ca90000
	s_mov_b32 s28, 0x6cab0000
	s_mov_b32 s29, 0
	v_readlane_b32 s11, v252, 1
	s_branch .LBB0_253
	s_nop 0
	s_nop 0
	s_nop 0
	s_nop 0
	s_nop 0
	s_nop 0
	s_nop 0
	s_nop 0
